# M1 prologue: kernel-pointer pairs already read from the LDS table copied from SGPRs instead of re-read (5 dependent LDS round trips less)
# baseline (speedup 1.0000x reference)
.LBB0_324:
	s_mov_b32 s4, s47
	v_mbcnt_lo_u32_b32 v44, -1, 0
	v_mbcnt_hi_u32_b32 v44, -1, v44
	s_mov_b32 s5, s73
	v_lshl_add_u32 v45, s4, 6, v44
	s_mov_b32 s4, s68
	s_mov_b32 s6, s69
	s_movk_i32 s5, 0x2000
	ds_read_b32 v1, v0 offset:704
	ds_read_b32 v2, v0 offset:708
	s_add_i32 s5, s5, 0
	v_readfirstlane_b32 s7, v45
	s_cmpk_gt_i32 s6, 0x43f
	s_waitcnt lgkmcnt(1)
	v_readfirstlane_b32 s8, v1
	ds_read_b32 v1, v0 offset:696
	s_waitcnt lgkmcnt(0)
	ds_read_b32 v1, v0 offset:700
	v_readfirstlane_b32 s9, v2
	s_waitcnt lgkmcnt(0)
	ds_read_b32 v1, v0 offset:624
	ds_read_b32 v2, v0 offset:628
	v_ashrrev_i32_e32 v38, 3, v45
	v_lshlrev_b32_e32 v47, 4, v44
	v_lshlrev_b32_e32 v46, 4, v45
	s_waitcnt lgkmcnt(1)
	v_readfirstlane_b32 s23, v1
	s_waitcnt lgkmcnt(0)
	v_readfirstlane_b32 s22, v2
	ds_read_b32 v1, v0 offset:632
	ds_read_b32 v2, v0 offset:636
	s_waitcnt lgkmcnt(1)
	v_readfirstlane_b32 s26, v1
	s_waitcnt lgkmcnt(0)
	v_readfirstlane_b32 s24, v2
	ds_read_b32 v1, v0 offset:624
	ds_read_b32 v2, v0 offset:628
	s_waitcnt lgkmcnt(1)
	v_readfirstlane_b32 s19, v1
	s_waitcnt lgkmcnt(0)
	v_readfirstlane_b32 s18, v2
	s_mov_b32 s17, s26
	s_mov_b32 s16, s24
	s_mov_b32 s21, s19
	s_mov_b32 s20, s18
	s_mov_b32 s13, s26
	s_mov_b32 s12, s24
	s_mov_b32 s11, s19
	s_mov_b32 s10, s18
	s_mov_b32 s15, s26
	s_mov_b32 s14, s24
	s_cbranch_scc1 .LBB0_335
	s_add_u32 s48, s23, s0
	s_addc_u32 s49, s22, s1
	global_load_dword v1, v0, s[48:49]
	s_add_u32 s22, s26, s0
	s_addc_u32 s23, s24, s1
	global_load_dword v2, v0, s[22:23]
	s_add_u32 s22, s19, s0
	s_addc_u32 s23, s18, s1
	global_load_dword v3, v0, s[22:23] offset:4
	s_add_u32 s18, s17, s0
	s_addc_u32 s19, s16, s1
	global_load_dword v4, v0, s[18:19] offset:4
	s_add_u32 s16, s21, s0
	s_addc_u32 s17, s20, s1
	global_load_dword v5, v0, s[16:17] offset:8
	s_add_u32 s16, s13, s0
	s_addc_u32 s17, s12, s1
	global_load_dword v6, v0, s[16:17] offset:8
	s_add_u32 s12, s11, s0
	s_addc_u32 s13, s10, s1
	global_load_dword v7, v0, s[12:13] offset:12
	s_add_u32 s10, s15, s0
	s_addc_u32 s11, s14, s1
	global_load_dword v17, v0, s[10:11] offset:12
	s_mov_b32 s10, 0x3fb8aa3b
	s_mov_b32 s15, 0xc2ce8ed0
	s_mov_b32 s16, 0x42b17218
	s_add_u32 s12, s8, 0x1c600000
	s_addc_u32 s13, s9, 0
	v_add_u32_e32 v20, 0x200, v45
	v_ashrrev_i32_e32 v54, 3, v20
	v_mov_b32_e32 v19, v0
	v_cvt_f32_i32_e32 v59, v38
	v_cvt_f32_i32_e32 v61, v54
	s_mov_b32 s18, s6
	s_waitcnt vmcnt(7)
	v_mul_f32_e32 v8, 0x3fb8aa3b, v1
	v_fma_f32 v9, v1, s10, -v8
	v_rndne_f32_e32 v10, v8
	v_fmac_f32_e32 v9, 0x32a5705f, v1
	v_sub_f32_e32 v8, v8, v10
	s_waitcnt vmcnt(6)
	v_mul_f32_e32 v11, 0x3fb8aa3b, v2
	v_add_f32_e32 v8, v8, v9
	v_fma_f32 v9, v2, s10, -v11
	v_rndne_f32_e32 v12, v11
	v_cvt_i32_f32_e32 v10, v10
	v_exp_f32_e32 v8, v8
	v_fmac_f32_e32 v9, 0x32a5705f, v2
	v_sub_f32_e32 v11, v11, v12
	s_waitcnt vmcnt(5)
	v_mul_f32_e32 v13, 0x3fb8aa3b, v3
	v_add_f32_e32 v9, v11, v9
	v_fma_f32 v11, v3, s10, -v13
	v_rndne_f32_e32 v14, v13
	v_cvt_i32_f32_e32 v12, v12
	v_exp_f32_e32 v9, v9
	v_fmac_f32_e32 v11, 0x32a5705f, v3
	v_sub_f32_e32 v13, v13, v14
	s_waitcnt vmcnt(4)
	v_mul_f32_e32 v15, 0x3fb8aa3b, v4
	v_add_f32_e32 v11, v13, v11
	v_fma_f32 v13, v4, s10, -v15
	v_rndne_f32_e32 v16, v15
	v_cvt_i32_f32_e32 v14, v14
	v_ldexp_f32 v8, v8, v10
	v_exp_f32_e32 v10, v11
	v_fmac_f32_e32 v13, 0x32a5705f, v4
	v_sub_f32_e32 v11, v15, v16
	v_cvt_i32_f32_e32 v15, v16
	s_waitcnt vmcnt(3)
	v_mul_f32_e32 v16, 0x3fb8aa3b, v5
	v_cmp_ngt_f32_e32 vcc, s15, v1
	v_add_f32_e32 v11, v11, v13
	v_fma_f32 v13, v5, s10, -v16
	v_cndmask_b32_e32 v8, 0, v8, vcc
	v_rndne_f32_e32 v18, v16
	v_cmp_nlt_f32_e32 vcc, s16, v1
	v_ldexp_f32 v1, v9, v12
	v_fmac_f32_e32 v13, 0x32a5705f, v5
	v_cndmask_b32_e32 v39, v211, v8, vcc
	v_exp_f32_e32 v8, v11
	v_sub_f32_e32 v9, v16, v18
	s_waitcnt vmcnt(2)
	v_mul_f32_e32 v12, 0x3fb8aa3b, v6
	v_cmp_ngt_f32_e32 vcc, s15, v2
	v_add_f32_e32 v9, v9, v13
	v_fma_f32 v13, v6, s10, -v12
	v_cndmask_b32_e32 v1, 0, v1, vcc
	v_rndne_f32_e32 v16, v12
	v_cmp_nlt_f32_e32 vcc, s16, v2
	v_cvt_i32_f32_e32 v11, v18
	v_exp_f32_e32 v2, v9
	v_cndmask_b32_e32 v48, v211, v1, vcc
	v_ldexp_f32 v1, v10, v14
	v_fmac_f32_e32 v13, 0x32a5705f, v6
	v_sub_f32_e32 v9, v12, v16
	v_cmp_ngt_f32_e32 vcc, s15, v3
	v_add_f32_e32 v9, v9, v13
	v_cvt_i32_f32_e32 v10, v16
	v_cndmask_b32_e32 v1, 0, v1, vcc
	v_cmp_nlt_f32_e32 vcc, s16, v3
	v_exp_f32_e32 v3, v9
	s_waitcnt vmcnt(1)
	v_mul_f32_e32 v12, 0x3fb8aa3b, v7
	v_cndmask_b32_e32 v49, v211, v1, vcc
	v_ldexp_f32 v1, v8, v15
	v_cmp_ngt_f32_e32 vcc, s15, v4
	v_fma_f32 v13, v7, s10, -v12
	v_fmac_f32_e32 v13, 0x32a5705f, v7
	v_cndmask_b32_e32 v1, 0, v1, vcc
	v_cmp_nlt_f32_e32 vcc, s16, v4
	v_lshlrev_b32_e32 v18, 3, v44
	v_and_b32_e32 v16, 56, v18
	v_cndmask_b32_e32 v50, v211, v1, vcc
	v_ldexp_f32 v1, v2, v11
	v_cmp_ngt_f32_e32 vcc, s15, v5
	v_rndne_f32_e32 v2, v12
	v_lshlrev_b32_e32 v42, 1, v16
	v_cndmask_b32_e32 v1, 0, v1, vcc
	v_cmp_nlt_f32_e32 vcc, s16, v5
	s_nop 1
	v_cndmask_b32_e32 v51, v211, v1, vcc
	v_ldexp_f32 v1, v3, v10
	v_sub_f32_e32 v3, v12, v2
	v_add_f32_e32 v3, v3, v13
	v_exp_f32_e32 v3, v3
	v_cvt_i32_f32_e32 v2, v2
	v_cmp_ngt_f32_e32 vcc, s15, v6
	s_nop 1
	v_cndmask_b32_e32 v1, 0, v1, vcc
	v_cmp_nlt_f32_e32 vcc, s16, v6
	v_lshlrev_b32_e32 v6, 1, v16
	s_nop 0
	v_cndmask_b32_e32 v52, v211, v1, vcc
	v_ldexp_f32 v1, v3, v2
	s_waitcnt vmcnt(0)
	v_mul_f32_e32 v2, 0x3fb8aa3b, v17
	v_fma_f32 v3, v17, s10, -v2
	s_ashr_i32 s10, s6, 2
	v_rndne_f32_e32 v4, v2
	s_mul_hi_i32 s11, s10, 0x78787879
	v_fmac_f32_e32 v3, 0x32a5705f, v17
	v_sub_f32_e32 v2, v2, v4
	s_lshr_b32 s14, s11, 31
	s_ashr_i32 s11, s11, 4
	v_add_f32_e32 v2, v2, v3
	s_add_i32 s11, s11, s14
	v_exp_f32_e32 v2, v2
	v_cvt_i32_f32_e32 v3, v4
	s_mul_i32 s14, s11, 0xffffffde
	s_add_i32 s14, s14, s10
	v_cmp_ngt_f32_e32 vcc, s15, v7
	s_mulk_i32 s11, 0x1100
	s_lshl_b32 s10, s14, 7
	v_cndmask_b32_e32 v1, 0, v1, vcc
	v_cmp_nlt_f32_e32 vcc, s16, v7
	s_add_i32 s14, s10, s11
	v_add_u32_e32 v4, s14, v38
	v_cndmask_b32_e32 v53, v211, v1, vcc
	v_ldexp_f32 v1, v2, v3
	v_mov_b64_e32 v[2:3], s[12:13]
	v_mad_i64_i32 v[4:5], s[10:11], v4, s60, v[2:3]
	s_lshl_b32 s10, s6, 7
	s_and_b32 s24, s10, 0x180
	v_mov_b32_e32 v7, v0
	v_lshl_add_u64 v[4:5], v[4:5], 0, s[24:25]
	v_lshl_add_u64 v[4:5], v[4:5], 0, v[6:7]
	v_add_co_u32_e32 v4, vcc, s78, v4
	s_nop 1
	v_addc_co_u32_e32 v5, vcc, 0, v5, vcc
	global_load_dwordx4 v[34:37], v[4:5], off offset:512
	global_load_dwordx4 v[12:15], v[4:5], off
	v_add_u32_e32 v4, s14, v54
	v_mad_i64_i32 v[2:3], s[10:11], v4, s60, v[2:3]
	v_lshl_add_u64 v[2:3], v[2:3], 0, s[24:25]
	v_lshl_add_u64 v[2:3], v[2:3], 0, v[6:7]
	v_add_co_u32_e32 v2, vcc, s78, v2
	s_ashr_i32 s10, s7, 8
	s_nop 0
	v_addc_co_u32_e32 v3, vcc, 0, v3, vcc
	global_load_dwordx4 v[8:11], v[2:3], off offset:512
	global_load_dwordx4 v[4:7], v[2:3], off
	v_cmp_ngt_f32_e32 vcc, s15, v17
	s_bfe_u32 s11, s7, 0x10006
	s_bfe_u32 s14, s7, 0x10007
	v_cndmask_b32_e32 v1, 0, v1, vcc
	v_cmp_nlt_f32_e32 vcc, s16, v17
	v_and_b32_e32 v2, 0xc0, v47
	v_lshlrev_b32_e32 v3, 1, v44
	v_cndmask_b32_e32 v55, v211, v1, vcc
	v_bfe_u32 v1, v18, 5, 1
	v_and_or_b32 v2, v18, 24, v2
	v_and_b32_e32 v3, 32, v3
	v_and_b32_e32 v18, 0x100, v18
	s_cmpk_lt_u32 s7, 0x100
	s_mov_b32 s7, 0x8000
	v_or3_b32 v2, v2, v3, v18
	s_cselect_b32 s7, 0x4000, s7
	v_lshl_or_b32 v3, s14, 9, v2
	s_add_i32 s7, s5, s7
	v_lshl_or_b32 v2, s11, 9, v2
	v_add_u32_e32 v57, s7, v2
	v_lshlrev_b32_e32 v2, 7, v44
	v_and_b32_e32 v2, 0xf80, v2
	v_add_u32_e32 v56, s5, v3
	v_lshl_or_b32 v2, s14, 12, v2
	v_mov_b32_e32 v3, v0
	v_lshl_add_u64 v[2:3], s[8:9], 0, v[2:3]
	s_lshl_b32 s24, s11, 6
	v_lshrrev_b32_e32 v18, 2, v44
	v_lshl_add_u64 v[2:3], v[2:3], 0, s[24:25]
	v_and_b32_e32 v18, 8, v18
	v_lshl_add_u64 v[2:3], v[2:3], 0, v[18:19]
	s_mov_b64 s[14:15], 0x1000000
	v_lshl_add_u64 v[40:41], v[2:3], 0, s[14:15]
	v_and_b32_e32 v3, 48, v38
	v_lshlrev_b32_e32 v18, 1, v38
	v_and_or_b32 v3, v18, 8, v3
	v_lshrrev_b32_e32 v18, 1, v38
	v_lshrrev_b32_e32 v3, 2, v3
	v_and_b32_e32 v19, 3, v38
	v_and_b32_e32 v17, 48, v47
	s_movk_i32 s7, 0xe000
	v_or_b32_e32 v3, v3, v1
	v_and_or_b32 v18, v18, 4, v19
	v_and_or_b32 v2, v46, s7, v17
	v_lshlrev_b32_e32 v3, 9, v3
	v_lshlrev_b32_e32 v18, 6, v18
	v_or3_b32 v18, v18, v3, v2
	v_and_b32_e32 v3, 48, v54
	v_lshlrev_b32_e32 v19, 1, v54
	v_and_or_b32 v3, v19, 8, v3
	v_lshrrev_b32_e32 v3, 2, v3
	v_sub_u32_e32 v2, 0x7f, v38
	v_lshrrev_b32_e32 v19, 1, v54
	v_or_b32_e32 v1, v3, v1
	v_and_b32_e32 v3, 3, v54
	v_cvt_f32_i32_e32 v58, v2
	v_lshlrev_b32_e32 v2, 4, v20
	v_lshlrev_b32_e32 v1, 9, v1
	v_and_or_b32 v3, v19, 4, v3
	v_and_b32_e32 v2, 0xffffe000, v2
	v_lshl_or_b32 v1, v3, 6, v1
	v_or3_b32 v17, v1, v2, v17
	v_sub_u32_e32 v1, 0x7f, v54
	v_cvt_f32_i32_e32 v60, v1
	v_mov_b32_e32 v2, v0
	v_mov_b32_e32 v3, v0
	s_add_i32 s7, s6, s4
	v_mov_b32_e32 v1, v0
	v_add_u32_e32 v62, s5, v18
	v_mov_b64_e32 v[20:21], v[2:3]
	v_mov_b64_e32 v[28:29], v[2:3]
	v_mov_b64_e32 v[24:25], v[2:3]
	v_mov_b64_e32 v[32:33], v[2:3]
	s_lshl_b32 s7, s7, 6
	s_lshl_b32 s11, s4, 6
	v_add_u32_e32 v63, s5, v17
	v_mov_b64_e32 v[18:19], v[0:1]
	v_mov_b64_e32 v[26:27], v[0:1]
	v_mov_b64_e32 v[22:23], v[0:1]
	v_mov_b64_e32 v[30:31], v[0:1]
	s_branch .LBB0_327
